# main: one static s_setprio 1 for waves 4-7 (younger half) at kernel entry
# baseline (speedup 1.0000x reference)
_Z7na_mainPKDF16_PKhS0_PKfS4_S4_S4_Pf:
	v_readfirstlane_b32 s36, v0
	s_nop 3
	s_lshr_b32 s36, s36, 6
	s_cmp_ge_u32 s36, 4
	s_cbranch_scc0 .Lprio_done
	s_setprio 1
.Lprio_done:
	s_lshl_b32 s3, s2, 5
	s_and_b32 s3, s3, 0xe0
	s_ashr_i32 s2, s2, 3
	s_add_i32 s3, s3, s2
	s_ashr_i32 s2, s3, 6
	s_lshl_b32 s3, s3, 5
	s_and_b32 s14, s3, 0x7e0
	v_mov_b32_e32 v1, 0x7c0
	s_load_dwordx8 s[4:11], s[0:1], 0x0
	s_load_dwordx2 s[18:19], s[0:1], 0x20
	s_load_dwordx2 s[28:29], s[0:1], 0x28
	s_load_dwordx2 s[34:35], s[0:1], 0x30
	s_load_dwordx2 s[30:31], s[0:1], 0x38
	v_med3_u32 v1, s14, 32, v1
	v_subrev_u32_e32 v97, 32, v1
	s_ashr_i32 s3, s2, 31
	v_lshlrev_b32_e32 v58, 1, v97
	s_lshl_b64 s[12:13], s[2:3], 12
	v_mov_b32_e32 v59, 0
	v_sub_u32_e32 v60, s14, v97
	v_lshl_add_u64 v[10:11], s[12:13], 0, v[58:59]
	v_lshlrev_b64 v[2:3], 9, v[10:11]
	v_lshl_or_b32 v22, v60, 6, v0
	s_waitcnt lgkmcnt(0)
	s_load_dword s32, s[28:29], 0x0
	v_and_b32_e32 v208, 31, v0
	v_lshlrev_b32_e32 v208, 5, v208
	global_load_dwordx4 v[192:195], v208, s[18:19]
	global_load_dwordx4 v[196:199], v208, s[18:19] offset:16
	v_lshl_add_u64 v[20:21], s[4:5], 0, v[2:3]
	v_ashrrev_i32_e32 v23, 31, v22
	v_lshl_add_u64 v[2:3], v[22:23], 4, v[20:21]
	global_load_dwordx4 v[12:15], v[2:3], off
	v_or_b32_e32 v28, 0x200, v22
	v_ashrrev_i32_e32 v29, 31, v28
	v_lshl_add_u64 v[2:3], v[28:29], 4, v[20:21]
	global_load_dwordx4 v[16:19], v[2:3], off
	v_or_b32_e32 v184, 0x400, v22
	v_ashrrev_i32_e32 v185, 31, v184
	v_lshl_add_u64 v[184:185], v[184:185], 4, v[20:21]
	v_or_b32_e32 v188, 0x600, v22
	v_ashrrev_i32_e32 v189, 31, v188
	v_lshl_add_u64 v[188:189], v[188:189], 4, v[20:21]
	global_load_dwordx4 v[184:187], v[184:185], off
	global_load_dwordx4 v[188:191], v[188:189], off
	v_lshrrev_b32_e32 v99, 6, v0
	v_and_b32_e32 v98, 63, v0
	v_lshlrev_b32_e32 v118, 13, v99
	v_lshl_or_b32 v58, v98, 4, v118
	v_and_b32_e32 v58, 0xfff0, v58
	v_add_u32_e32 v251, 0x1000, v58
	s_movk_i32 s15, 0x1000
	v_lshl_add_u64 v[24:25], s[6:7], 0, v[58:59]
	v_or_b32_e32 v32, 0x400, v22
	v_or_b32_e32 v62, 0x600, v22
	v_add_co_u32_e32 v64, vcc, s15, v24
	s_mov_b64 s[12:13], 0x1000
	s_mov_b64 s[16:17], 0x1800
	v_lshlrev_b32_e32 v72, 1, v60
	v_lshrrev_b32_e32 v23, 5, v22
	v_and_b32_e32 v34, 32, v22
	v_ashrrev_i32_e32 v33, 31, v32
	v_ashrrev_i32_e32 v63, 31, v62
	v_addc_co_u32_e32 v65, vcc, 0, v25, vcc
	global_load_dwordx4 v[6:9], v58, s[6:7] offset:1024
	global_load_dwordx4 v[2:5], v58, s[6:7]
	global_load_dwordx4 v[54:57], v58, s[6:7] offset:3072
	global_load_dwordx4 v[50:53], v58, s[6:7] offset:2048
	v_lshrrev_b32_e32 v58, 6, v22
	v_bfe_u32 v73, v22, 8, 2
	v_lshl_add_u64 v[26:27], v[24:25], 0, s[12:13]
	v_lshl_add_u64 v[24:25], v[24:25], 0, s[16:17]
	v_cmp_ne_u32_e32 vcc, 0, v34
	v_sub_u32_e32 v75, v23, v72
	global_load_dwordx4 v[42:45], v251, s[6:7]
	global_load_dwordx4 v[46:49], v251, s[6:7] offset:1024
	global_load_dwordx4 v[34:37], v251, s[6:7] offset:2048
	global_load_dwordx4 v[38:41], v251, s[6:7] offset:3072
	v_mov_b32_e32 v61, 0x60
	v_cndmask_b32_e32 v74, 0, v61, vcc
	v_add_u32_e32 v33, v74, v58
	v_lshlrev_b32_e32 v64, 2, v33
	v_bfe_u32 v96, v0, 4, 1
	v_and_b32_e32 v100, 15, v0
	v_mov_b32_e32 v30, v59
	v_mov_b32_e32 v31, v59
	v_and_b32_e32 v64, 12, v64
	v_mul_u32_u24_e32 v29, 0xc000, v96
	v_bitop3_b32 v64, v64, v100, v73 bitop3:0x36
	v_lshl_or_b32 v64, v64, 4, v29
	v_lshlrev_b32_e32 v63, 1, v75
	v_lshl_add_u32 v33, v33, 8, v64
	v_bfe_u32 v71, v0, 1, 4
	v_and_b32_e32 v70, 32, v0
	v_lshlrev_b32_e32 v1, 3, v0
	v_lshrrev_b32_e32 v58, 1, v75
	v_and_b32_e32 v1, 8, v1
	v_add_lshl_u32 v58, v58, v70, 8
	v_lshlrev_b32_e32 v121, 3, v99
	v_bfe_u32 v101, v0, 4, 2
	v_lshlrev_b32_e32 v102, 2, v101
	v_and_b32_e32 v116, 31, v0
	v_bfe_u32 v119, v0, 5, 1
	v_lshlrev_b32_e32 v124, 1, v119
	v_lshlrev_b32_e32 v117, 8, v116
	v_lshrrev_b32_e32 v95, 4, v0
	s_movk_i32 s16, 0x60
	s_mov_b32 s17, 0xc000
	v_and_b32_e32 v211, 3, v99
	v_lshrrev_b32_e32 v212, 2, v99
	v_lshl_or_b32 v211, v211, 2, v212
	v_xor_b32_e32 v213, v100, v211
	v_mul_u32_u24_e32 v214, 0x60, v119
	v_add3_u32 v214, v214, v60, v99
	v_mul_u32_u24_e32 v215, 0xc000, v96
	v_lshl_add_u32 v214, v214, 8, v215
	v_lshl_or_b32 v220, v213, 4, v214
	v_xor_b32_e32 v221, 32, v220
	v_xor_b32_e32 v216, v71, v211
	v_lshl_add_u32 v217, v119, 5, v99
	v_lshlrev_b32_e32 v217, 8, v217
	v_lshl_or_b32 v216, v216, 4, v217
	v_or_b32_e32 v216, v216, v1
	v_add_u32_e32 v222, 0x23800, v216
	v_xor_b32_e32 v223, 32, v222
	s_waitcnt vmcnt(11)
	ds_write_b128 v220, v[12:15]
	v_fma_mix_f32 v200, v192, v12, 0 op_sel_hi:[0,1,0]
	v_fma_mix_f32 v201, v193, v12, 0 op_sel:[0,1,0] op_sel_hi:[0,1,0]
	v_cvt_f32_f16_e32 v211, v12
	v_cvt_f32_f16_sdwa v212, v12 dst_sel:DWORD dst_unused:UNUSED_PAD src0_sel:WORD_1
	v_fma_mix_f32 v200, v194, v13, v200 op_sel_hi:[0,1,0]
	v_fma_mix_f32 v201, v195, v13, v201 op_sel:[0,1,0] op_sel_hi:[0,1,0]
	v_cvt_f32_f16_e32 v213, v13
	v_cvt_f32_f16_sdwa v214, v13 dst_sel:DWORD dst_unused:UNUSED_PAD src0_sel:WORD_1
	v_fma_mix_f32 v200, v196, v14, v200 op_sel_hi:[0,1,0]
	v_fma_mix_f32 v201, v197, v14, v201 op_sel:[0,1,0] op_sel_hi:[0,1,0]
	v_cvt_f32_f16_e32 v215, v14
	v_cvt_f32_f16_sdwa v216, v14 dst_sel:DWORD dst_unused:UNUSED_PAD src0_sel:WORD_1
	v_fma_mix_f32 v200, v198, v15, v200 op_sel_hi:[0,1,0]
	v_fma_mix_f32 v201, v199, v15, v201 op_sel:[0,1,0] op_sel_hi:[0,1,0]
	v_cvt_f32_f16_e32 v217, v15
	v_cvt_f32_f16_sdwa v218, v15 dst_sel:DWORD dst_unused:UNUSED_PAD src0_sel:WORD_1
	v_cvt_pk_fp8_f32 v224, v211, v212
	v_cvt_pk_fp8_f32 v225, v215, v216
	v_cvt_pk_fp8_f32 v224, v213, v214 op_sel:[0,0,1]
	v_cvt_pk_fp8_f32 v225, v217, v218 op_sel:[0,0,1]
	s_nop 0
	ds_write_b64 v222, v[224:225]
	s_waitcnt vmcnt(10)
	ds_write_b128 v221, v[16:19] offset:2048
	v_fma_mix_f32 v202, v192, v16, 0 op_sel_hi:[0,1,0]
	v_fma_mix_f32 v203, v193, v16, 0 op_sel:[0,1,0] op_sel_hi:[0,1,0]
	v_cvt_f32_f16_e32 v211, v16
	v_cvt_f32_f16_sdwa v212, v16 dst_sel:DWORD dst_unused:UNUSED_PAD src0_sel:WORD_1
	v_fma_mix_f32 v202, v194, v17, v202 op_sel_hi:[0,1,0]
	v_fma_mix_f32 v203, v195, v17, v203 op_sel:[0,1,0] op_sel_hi:[0,1,0]
	v_cvt_f32_f16_e32 v213, v17
	v_cvt_f32_f16_sdwa v214, v17 dst_sel:DWORD dst_unused:UNUSED_PAD src0_sel:WORD_1
	v_fma_mix_f32 v202, v196, v18, v202 op_sel_hi:[0,1,0]
	v_fma_mix_f32 v203, v197, v18, v203 op_sel:[0,1,0] op_sel_hi:[0,1,0]
	v_cvt_f32_f16_e32 v215, v18
	v_cvt_f32_f16_sdwa v216, v18 dst_sel:DWORD dst_unused:UNUSED_PAD src0_sel:WORD_1
	v_fma_mix_f32 v202, v198, v19, v202 op_sel_hi:[0,1,0]
	v_fma_mix_f32 v203, v199, v19, v203 op_sel:[0,1,0] op_sel_hi:[0,1,0]
	v_cvt_f32_f16_e32 v217, v19
	v_cvt_f32_f16_sdwa v218, v19 dst_sel:DWORD dst_unused:UNUSED_PAD src0_sel:WORD_1
	v_cvt_pk_fp8_f32 v226, v211, v212
	v_cvt_pk_fp8_f32 v227, v215, v216
	v_cvt_pk_fp8_f32 v226, v213, v214 op_sel:[0,0,1]
	v_cvt_pk_fp8_f32 v227, v217, v218 op_sel:[0,0,1]
	s_nop 0
	ds_write_b64 v223, v[226:227] offset:2048
	s_waitcnt vmcnt(9)
	ds_write_b128 v220, v[184:187] offset:4096
	v_fma_mix_f32 v204, v192, v184, 0 op_sel_hi:[0,1,0]
	v_fma_mix_f32 v205, v193, v184, 0 op_sel:[0,1,0] op_sel_hi:[0,1,0]
	v_cvt_f32_f16_e32 v211, v184
	v_cvt_f32_f16_sdwa v212, v184 dst_sel:DWORD dst_unused:UNUSED_PAD src0_sel:WORD_1
	v_fma_mix_f32 v204, v194, v185, v204 op_sel_hi:[0,1,0]
	v_fma_mix_f32 v205, v195, v185, v205 op_sel:[0,1,0] op_sel_hi:[0,1,0]
	v_cvt_f32_f16_e32 v213, v185
	v_cvt_f32_f16_sdwa v214, v185 dst_sel:DWORD dst_unused:UNUSED_PAD src0_sel:WORD_1
	v_fma_mix_f32 v204, v196, v186, v204 op_sel_hi:[0,1,0]
	v_fma_mix_f32 v205, v197, v186, v205 op_sel:[0,1,0] op_sel_hi:[0,1,0]
	v_cvt_f32_f16_e32 v215, v186
	v_cvt_f32_f16_sdwa v216, v186 dst_sel:DWORD dst_unused:UNUSED_PAD src0_sel:WORD_1
	v_fma_mix_f32 v204, v198, v187, v204 op_sel_hi:[0,1,0]
	v_fma_mix_f32 v205, v199, v187, v205 op_sel:[0,1,0] op_sel_hi:[0,1,0]
	v_cvt_f32_f16_e32 v217, v187
	v_cvt_f32_f16_sdwa v218, v187 dst_sel:DWORD dst_unused:UNUSED_PAD src0_sel:WORD_1
	v_cvt_pk_fp8_f32 v228, v211, v212
	v_cvt_pk_fp8_f32 v229, v215, v216
	v_cvt_pk_fp8_f32 v228, v213, v214 op_sel:[0,0,1]
	v_cvt_pk_fp8_f32 v229, v217, v218 op_sel:[0,0,1]
	s_nop 0
	ds_write_b64 v222, v[228:229] offset:4096
	s_waitcnt vmcnt(8)
	ds_write_b128 v221, v[188:191] offset:6144
	v_fma_mix_f32 v206, v192, v188, 0 op_sel_hi:[0,1,0]
	v_fma_mix_f32 v207, v193, v188, 0 op_sel:[0,1,0] op_sel_hi:[0,1,0]
	v_cvt_f32_f16_e32 v211, v188
	v_cvt_f32_f16_sdwa v212, v188 dst_sel:DWORD dst_unused:UNUSED_PAD src0_sel:WORD_1
	v_fma_mix_f32 v206, v194, v189, v206 op_sel_hi:[0,1,0]
	v_fma_mix_f32 v207, v195, v189, v207 op_sel:[0,1,0] op_sel_hi:[0,1,0]
	v_cvt_f32_f16_e32 v213, v189
	v_cvt_f32_f16_sdwa v214, v189 dst_sel:DWORD dst_unused:UNUSED_PAD src0_sel:WORD_1
	v_fma_mix_f32 v206, v196, v190, v206 op_sel_hi:[0,1,0]
	v_fma_mix_f32 v207, v197, v190, v207 op_sel:[0,1,0] op_sel_hi:[0,1,0]
	v_cvt_f32_f16_e32 v215, v190
	v_cvt_f32_f16_sdwa v216, v190 dst_sel:DWORD dst_unused:UNUSED_PAD src0_sel:WORD_1
	v_fma_mix_f32 v206, v198, v191, v206 op_sel_hi:[0,1,0]
	v_fma_mix_f32 v207, v199, v191, v207 op_sel:[0,1,0] op_sel_hi:[0,1,0]
	v_cvt_f32_f16_e32 v217, v191
	v_cvt_f32_f16_sdwa v218, v191 dst_sel:DWORD dst_unused:UNUSED_PAD src0_sel:WORD_1
	v_cvt_pk_fp8_f32 v230, v211, v212
	v_cvt_pk_fp8_f32 v231, v215, v216
	v_cvt_pk_fp8_f32 v230, v213, v214 op_sel:[0,0,1]
	v_cvt_pk_fp8_f32 v231, v217, v218 op_sel:[0,0,1]
	s_nop 0
	ds_write_b64 v223, v[230:231] offset:6144
	v_add_f32_e32 v200, v200, v201
	v_add_f32_e32 v202, v202, v203
	v_add_f32_e32 v204, v204, v205
	v_add_f32_e32 v206, v206, v207
	v_lshlrev_b32_e32 v208, 7, v119
	v_lshl_add_u32 v208, v99, 2, v208
	v_add_u32_e32 v208, 0x27800, v208
	v_add_f32_dpp v200, v200, v200 quad_perm:[1,0,3,2] row_mask:0xf bank_mask:0xf
	v_add_f32_dpp v202, v202, v202 quad_perm:[1,0,3,2] row_mask:0xf bank_mask:0xf
	v_add_f32_dpp v204, v204, v204 quad_perm:[1,0,3,2] row_mask:0xf bank_mask:0xf
	v_add_f32_dpp v206, v206, v206 quad_perm:[1,0,3,2] row_mask:0xf bank_mask:0xf
	v_add_f32_dpp v200, v200, v200 quad_perm:[2,3,0,1] row_mask:0xf bank_mask:0xf
	v_add_f32_dpp v202, v202, v202 quad_perm:[2,3,0,1] row_mask:0xf bank_mask:0xf
	v_add_f32_dpp v204, v204, v204 quad_perm:[2,3,0,1] row_mask:0xf bank_mask:0xf
	v_add_f32_dpp v206, v206, v206 quad_perm:[2,3,0,1] row_mask:0xf bank_mask:0xf
	v_add_f32_dpp v200, v200, v200 row_half_mirror row_mask:0xf bank_mask:0xf
	v_add_f32_dpp v202, v202, v202 row_half_mirror row_mask:0xf bank_mask:0xf
	v_add_f32_dpp v204, v204, v204 row_half_mirror row_mask:0xf bank_mask:0xf
	v_add_f32_dpp v206, v206, v206 row_half_mirror row_mask:0xf bank_mask:0xf
	v_add_f32_dpp v200, v200, v200 row_mirror row_mask:0xf bank_mask:0xf
	v_add_f32_dpp v202, v202, v202 row_mirror row_mask:0xf bank_mask:0xf
	v_add_f32_dpp v204, v204, v204 row_mirror row_mask:0xf bank_mask:0xf
	v_add_f32_dpp v206, v206, v206 row_mirror row_mask:0xf bank_mask:0xf
	v_add_f32_dpp v200, v200, v200 row_bcast:15 row_mask:0xa bank_mask:0xf
	v_add_f32_dpp v202, v202, v202 row_bcast:15 row_mask:0xa bank_mask:0xf
	v_add_f32_dpp v204, v204, v204 row_bcast:15 row_mask:0xa bank_mask:0xf
	v_add_f32_dpp v206, v206, v206 row_bcast:15 row_mask:0xa bank_mask:0xf
	s_mov_b32 exec_lo, 0xffff0000
	s_mov_b32 exec_hi, 0xffff0000
	ds_write_b32 v208, v200
	ds_write_b32 v208, v202 offset:32
	ds_write_b32 v208, v204 offset:64
	ds_write_b32 v208, v206 offset:96
	s_mov_b64 exec, -1
	v_lshlrev_b32_e32 v201, 7, v99
	v_lshl_or_b32 v201, v119, 4, v201
	global_load_dwordx4 v[184:187], v201, s[10:11]
	global_load_dwordx4 v[188:191], v201, s[10:11] offset:32
	global_load_dwordx4 v[192:195], v201, s[10:11] offset:64
	global_load_dwordx4 v[196:199], v201, s[10:11] offset:96
	v_cmp_lt_i32_e32 vcc, v121, v60
	s_nop 0
	v_mov_b32_e32 v15, v59
	v_cndmask_b32_e64 v12, 32, 0, vcc
	v_add_u32_e32 v16, v12, v121
	v_or_b32_e32 v12, v16, v101
	v_lshlrev_b32_e32 v58, 1, v12
	v_lshrrev_b32_e32 v12, 5, v0
	v_and_b32_e32 v12, 2, v12
	v_bitop3_b32 v14, v102, v100, v12 bitop3:0x36
	v_lshl_add_u64 v[12:13], v[10:11], 0, v[58:59]
	v_lshlrev_b64 v[12:13], 9, v[12:13]
	v_lshlrev_b32_e32 v16, 8, v16
	v_lshl_add_u64 v[12:13], s[4:5], 0, v[12:13]
	v_lshlrev_b32_e32 v14, 4, v14
	v_readfirstlane_b32 s6, v16
	v_add_u32_e32 v17, 0xc000, v16
	v_lshl_add_u64 v[12:13], v[12:13], 0, v[14:15]
	s_mov_b32 m0, s6
	s_mov_b64 s[6:7], 0x100
	v_readfirstlane_b32 s12, v17
	global_load_lds_dwordx4 v[12:13], off
	v_lshl_add_u64 v[12:13], v[12:13], 0, s[6:7]
	s_mov_b32 m0, s12
	v_or_b32_e32 v58, 1, v58
	global_load_lds_dwordx4 v[12:13], off
	v_lshl_add_u64 v[12:13], v[10:11], 0, v[58:59]
	v_lshlrev_b64 v[12:13], 9, v[12:13]
	v_lshl_add_u64 v[12:13], s[4:5], 0, v[12:13]
	v_lshl_add_u64 v[12:13], v[12:13], 0, v[14:15]
	v_add_u32_e32 v14, 0x6000, v16
	v_bfe_u32 v61, v0, 2, 2
	v_readfirstlane_b32 s12, v14
	v_add_u32_e32 v14, 0x12000, v16
	s_mov_b32 m0, s12
	v_readfirstlane_b32 s12, v14
	global_load_lds_dwordx4 v[12:13], off
	v_lshl_add_u64 v[12:13], v[12:13], 0, s[6:7]
	s_mov_b32 m0, s12
	v_add_u32_e32 v18, 0x23800, v117
	global_load_lds_dwordx4 v[12:13], off
	v_or_b32_e32 v12, 4, v121
	v_cmp_lt_i32_e32 vcc, v12, v60
	s_nop 1
	v_cndmask_b32_e64 v13, 32, 0, vcc
	v_add_u32_e32 v16, v13, v12
	v_or_b32_e32 v13, v16, v101
	v_lshlrev_b32_e32 v58, 1, v13
	v_bfe_u32 v12, v12, 2, 2
	v_bitop3_b32 v14, v102, v100, v12 bitop3:0x36
	v_lshl_add_u64 v[12:13], v[10:11], 0, v[58:59]
	v_lshlrev_b64 v[12:13], 9, v[12:13]
	v_lshlrev_b32_e32 v16, 8, v16
	v_lshl_add_u64 v[12:13], s[4:5], 0, v[12:13]
	v_lshlrev_b32_e32 v14, 4, v14
	v_readfirstlane_b32 s12, v16
	v_add_u32_e32 v17, 0xc000, v16
	v_lshl_add_u64 v[12:13], v[12:13], 0, v[14:15]
	s_mov_b32 m0, s12
	v_readfirstlane_b32 s12, v17
	v_or_b32_e32 v58, 1, v58
	global_load_lds_dwordx4 v[12:13], off
	v_lshl_add_u64 v[12:13], v[12:13], 0, s[6:7]
	s_mov_b32 m0, s12
	v_lshl_add_u64 v[10:11], v[10:11], 0, v[58:59]
	global_load_lds_dwordx4 v[12:13], off
	v_lshlrev_b64 v[10:11], 9, v[10:11]
	v_add_u32_e32 v12, 0x6000, v16
	v_lshl_add_u64 v[10:11], s[4:5], 0, v[10:11]
	v_readfirstlane_b32 s4, v12
	v_add_u32_e32 v12, 0x12000, v16
	v_lshl_add_u64 v[10:11], v[10:11], 0, v[14:15]
	s_mov_b32 m0, s4
	v_readfirstlane_b32 s4, v12
	global_load_lds_dwordx4 v[10:11], off
	v_lshl_add_u64 v[10:11], v[10:11], 0, s[6:7]
	s_mov_b32 m0, s4
	s_nop 0
	global_load_lds_dwordx4 v[10:11], off
	s_waitcnt lgkmcnt(0)
	s_barrier
	v_lshlrev_b32_e32 v10, 2, v0
	v_and_b32_e32 v94, 12, v10
	v_or_b32_e32 v120, v94, v61
	v_bitop3_b32 v10, v124, v94, v61 bitop3:0x1e
	v_lshl_or_b32 v14, v10, 4, v18
	v_bitop3_b32 v10, v124, v120, 1 bitop3:0x36
	v_lshl_or_b32 v19, v10, 4, v18
	ds_read_b128 v[10:13], v14
	ds_read_b128 v[62:65], v14 offset:8192
	ds_read_b128 v[14:17], v19
	ds_read_b128 v[66:69], v19 offset:8192
	v_bitop3_b32 v19, v124, v120, 4 bitop3:0x36
	v_lshl_or_b32 v19, v19, 4, v18
	v_bitop3_b32 v20, v124, v120, 5 bitop3:0x36
	v_lshl_or_b32 v20, v20, 4, v18
	ds_read_b128 v[70:73], v19
	ds_read_b128 v[78:81], v19 offset:8192
	ds_read_b128 v[74:77], v20
	ds_read_b128 v[82:85], v20 offset:8192
	v_bitop3_b32 v19, v124, v120, 8 bitop3:0x36
	v_lshl_or_b32 v19, v19, 4, v18
	v_bitop3_b32 v20, v124, v120, 9 bitop3:0x36
	v_lshl_or_b32 v20, v20, 4, v18
	ds_read_b128 v[86:89], v19
	ds_read_b128 v[104:107], v19 offset:8192
	ds_read_b128 v[90:93], v20
	ds_read_b128 v[108:111], v20 offset:8192
	v_bitop3_b32 v19, v124, v120, 12 bitop3:0x36
	v_lshl_or_b32 v19, v19, 4, v18
	v_bitop3_b32 v20, v124, v120, 13 bitop3:0x36
	v_lshl_or_b32 v18, v20, 4, v18
	ds_read_b128 v[126:129], v19
	ds_read_b128 v[134:137], v19 offset:8192
	ds_read_b128 v[130:133], v18
	ds_read_b128 v[138:141], v18 offset:8192
	v_mov_b32_e32 v103, 0x7f
	v_lshlrev_b32_e32 v58, 7, v99
	v_or_b32_e32 v122, 0x18000, v117
	s_waitcnt vmcnt(18) lgkmcnt(0)
	v_mfma_scale_f32_32x32x64_f8f6f4 v[18:33], v[2:9], v[10:17], 0, v103, v103 op_sel_hi:[0,0,0]
	v_lshlrev_b32_e32 v125, 3, v119
	v_or_b32_e32 v123, 0x1a000, v117
	v_mfma_scale_f32_32x32x64_f8f6f4 v[2:17], v[2:9], v[62:69], 0, v103, v103 op_sel_hi:[0,0,0]
	v_and_b32_e32 v62, 12, v95
	s_waitcnt vmcnt(16)
	v_mfma_scale_f32_32x32x64_f8f6f4 v[18:33], v[50:57], v[70:77], v[18:33], v103, v103 op_sel_hi:[0,0,0]
	v_mfma_scale_f32_32x32x64_f8f6f4 v[2:17], v[50:57], v[78:85], v[2:17], v103, v103 op_sel_hi:[0,0,0]
	s_brev_b32 s10, 60
	v_lshlrev_b32_e32 v58, 6, v0
	v_and_b32_e32 v58, 0x4000, v58
	v_or3_b32 v63, v122, v58, v125
	v_or3_b32 v58, v123, v58, v125
	s_waitcnt vmcnt(14)
	v_mfma_scale_f32_32x32x64_f8f6f4 v[18:33], v[42:49], v[86:93], v[18:33], v103, v103 op_sel_hi:[0,0,0]
	v_mfma_scale_f32_32x32x64_f8f6f4 v[2:17], v[42:49], v[104:111], v[2:17], v103, v103 op_sel_hi:[0,0,0]
	s_nop 0
	s_waitcnt vmcnt(12)
	v_mfma_scale_f32_32x32x64_f8f6f4 v[2:17], v[34:41], v[134:141], v[2:17], v103, v103 op_sel_hi:[0,0,0]
	v_mfma_scale_f32_32x32x64_f8f6f4 v[18:33], v[34:41], v[126:133], v[18:33], v103, v103 op_sel_hi:[0,0,0]
	s_waitcnt vmcnt(8)
	s_nop 15
	s_nop 1
	v_fma_f32 v2, v2, s10, v184
	v_fma_f32 v3, v3, s10, v185
	v_fma_f32 v4, v4, s10, v186
	v_fma_f32 v5, v5, s10, v187
	v_cvt_pk_f16_f32 v2, v2, v3
	v_cvt_pk_f16_f32 v3, v4, v5
	v_bitop3_b32 v4, v95, v120, 12 bitop3:0x6c
	v_pk_fma_f32 v[18:19], v[18:19], s[10:11], v[184:185] op_sel_hi:[1,0,1]
	v_pk_fma_f32 v[20:21], v[20:21], s[10:11], v[186:187] op_sel_hi:[1,0,1]
	v_lshlrev_b32_e32 v4, 4, v4
	v_cvt_pk_f16_f32 v18, v18, v19
	v_cvt_pk_f16_f32 v19, v20, v21
	v_or_b32_e32 v5, v63, v4
	v_or_b32_e32 v4, v58, v4
	ds_write_b64 v5, v[18:19]
	ds_write_b64 v4, v[2:3]
	v_pk_fma_f32 v[2:3], v[22:23], s[10:11], v[188:189] op_sel_hi:[1,0,1]
	v_pk_fma_f32 v[4:5], v[6:7], s[10:11], v[188:189] op_sel_hi:[1,0,1]
	v_pk_fma_f32 v[6:7], v[24:25], s[10:11], v[190:191] op_sel_hi:[1,0,1]
	v_cvt_pk_f16_f32 v2, v2, v3
	v_cvt_pk_f16_f32 v3, v6, v7
	v_pk_fma_f32 v[6:7], v[8:9], s[10:11], v[190:191] op_sel_hi:[1,0,1]
	v_cvt_pk_f16_f32 v4, v4, v5
	v_cvt_pk_f16_f32 v5, v6, v7
	v_bitop3_b32 v6, v62, v120, 1 bitop3:0x36
	v_lshlrev_b32_e32 v6, 4, v6
	v_or_b32_e32 v7, v63, v6
	ds_write_b64 v7, v[2:3]
	v_or_b32_e32 v2, v58, v6
	ds_write_b64 v2, v[4:5]
	v_pk_fma_f32 v[2:3], v[26:27], s[10:11], v[192:193] op_sel_hi:[1,0,1]
	v_pk_fma_f32 v[6:7], v[28:29], s[10:11], v[194:195] op_sel_hi:[1,0,1]
	v_cvt_pk_f16_f32 v2, v2, v3
	v_pk_fma_f32 v[4:5], v[10:11], s[10:11], v[192:193] op_sel_hi:[1,0,1]
	v_cvt_pk_f16_f32 v3, v6, v7
	v_pk_fma_f32 v[6:7], v[12:13], s[10:11], v[194:195] op_sel_hi:[1,0,1]
	v_cvt_pk_f16_f32 v4, v4, v5
	v_cvt_pk_f16_f32 v5, v6, v7
	v_bitop3_b32 v6, v62, v120, 2 bitop3:0x36
	v_lshlrev_b32_e32 v6, 4, v6
	v_or_b32_e32 v7, v63, v6
	ds_write_b64 v7, v[2:3]
	v_or_b32_e32 v2, v58, v6
	ds_write_b64 v2, v[4:5]
	v_pk_fma_f32 v[2:3], v[30:31], s[10:11], v[196:197] op_sel_hi:[1,0,1]
	v_pk_fma_f32 v[6:7], v[32:33], s[10:11], v[198:199] op_sel_hi:[1,0,1]
	v_cvt_pk_f16_f32 v2, v2, v3
	v_pk_fma_f32 v[4:5], v[14:15], s[10:11], v[196:197] op_sel_hi:[1,0,1]
	v_cvt_pk_f16_f32 v3, v6, v7
	v_pk_fma_f32 v[6:7], v[16:17], s[10:11], v[198:199] op_sel_hi:[1,0,1]
	v_cvt_pk_f16_f32 v4, v4, v5
	v_cvt_pk_f16_f32 v5, v6, v7
	v_bitop3_b32 v6, v62, v120, 3 bitop3:0x36
	v_lshlrev_b32_e32 v6, 4, v6
	v_or_b32_e32 v7, v63, v6
	ds_write_b64 v7, v[2:3]
	v_or_b32_e32 v2, v58, v6
	ds_write_b64 v2, v[4:5]
	s_waitcnt vmcnt(0) lgkmcnt(0)
	s_barrier
	v_and_b32_e32 v236, 1, v101
	v_lshrrev_b32_e32 v237, 1, v101
	v_xor_b32_e32 v237, v237, v236
	v_lshl_or_b32 v236, v236, 1, v237
	v_lshrrev_b32_e32 v27, 8, v0
	v_lshrrev_b32_e32 v3, 3, v0
	v_and_b32_e32 v3, 16, v3
	v_mul_u32_u24_e32 v28, 0x60, v27
	v_lshlrev_b32_e32 v26, 5, v27
	v_or_b32_e32 v146, v3, v100
	v_or_b32_e32 v147, v28, v100
	v_or_b32_e32 v4, v146, v26
	v_lshlrev_b32_e32 v209, 2, v4
	v_add_u32_e32 v209, 0x27800, v209
	v_lshlrev_b32_e32 v4, 8, v4
	v_or_b32_e32 v5, 0x18000, v4
	v_bitop3_b32 v11, v236, v120, 12 bitop3:0x36
	v_or_b32_e32 v95, 0x1c000, v4
	v_lshlrev_b32_e32 v29, 3, v101
	v_bitop3_b32 v6, v236, v94, v61 bitop3:0x1e
	v_bitop3_b32 v8, v236, v120, 4 bitop3:0x36
	v_bitop3_b32 v10, v236, v120, 8 bitop3:0x36
	v_lshlrev_b32_e32 v94, 4, v11
	v_lshlrev_b32_e32 v6, 4, v6
	v_lshlrev_b32_e32 v8, 4, v8
	v_lshlrev_b32_e32 v58, 4, v10
	v_or_b32_e32 v7, v5, v6
	v_or_b32_e32 v9, v5, v8
	v_or_b32_e32 v10, v5, v58
	v_or_b32_e32 v5, v5, v94
	v_or_b32_e32 v6, v95, v6
	v_or_b32_e32 v60, v95, v8
	ds_read_b128 v[22:25], v7
	ds_read_b128 v[18:21], v9
	ds_read_b128 v[14:17], v10
	ds_read_b128 v[10:13], v5
	ds_read_b128 v[6:9], v6
	ds_read_b128 v[2:5], v60
	v_bfe_u32 v103, v0, 6, 1
	s_movk_i32 s5, 0x2000
	v_mad_u32_u24 v44, v103, 48, v147
	v_lshlrev_b32_e32 v60, 8, v44
	v_lshlrev_b32_e32 v44, 2, v44
	v_or_b32_e32 v35, v95, v58
	v_lshlrev_b32_e32 v58, 14, v99
	v_and_b32_e32 v44, 12, v44
	v_or_b32_e32 v56, v44, v61
	v_bitop3_b32 v44, v236, v44, v61 bitop3:0x1e
	v_lshl_add_u64 v[32:33], s[8:9], 0, v[58:59]
	v_lshlrev_b32_e32 v58, 4, v98
	v_or_b32_e32 v36, v95, v94
	v_lshl_add_u64 v[88:89], v[32:33], 0, v[58:59]
	v_lshl_or_b32 v57, v44, 4, v60
	ds_read_b128 v[40:43], v35
	ds_read_b128 v[106:109], v36
	global_load_dwordx4 v[36:39], v[88:89], off
	global_load_dwordx4 v[32:35], v[88:89], off offset:1024
	ds_read_b128 v[44:47], v57
	v_bitop3_b32 v48, v236, v56, 4 bitop3:0x36
	v_lshl_or_b32 v62, v48, 4, v60
	ds_read_b128 v[48:51], v62
	v_bitop3_b32 v52, v236, v56, 8 bitop3:0x36
	v_lshl_or_b32 v63, v52, 4, v60
	ds_read_b128 v[52:55], v63
	s_waitcnt lgkmcnt(0)
	v_mfma_f32_16x16x32_f16 v[44:47], v[44:47], v[22:25], 0
	v_bitop3_b32 v64, v236, v56, 12 bitop3:0x36
	ds_read_b128 v[56:59], v57 offset:49152
	v_lshl_or_b32 v60, v64, 4, v60
	v_mfma_f32_16x16x32_f16 v[44:47], v[48:51], v[18:21], v[44:47]
	ds_read_b128 v[68:71], v60
	ds_read_b128 v[72:75], v62 offset:49152
	v_mad_u32_u24 v104, v103, 3, 1
	v_lshlrev_b32_e32 v132, 4, v104
	v_mfma_f32_16x16x32_f16 v[44:47], v[52:55], v[14:17], v[44:47]
	v_add_u32_e32 v52, v132, v147
	global_load_dwordx4 v[64:67], v[88:89], off offset:2048
	global_load_dwordx4 v[48:51], v[88:89], off offset:3072
	ds_read_b128 v[76:79], v63 offset:49152
	ds_read_b128 v[80:83], v60 offset:49152
	s_waitcnt lgkmcnt(3)
	v_mfma_f32_16x16x32_f16 v[44:47], v[68:71], v[10:13], v[44:47]
	v_lshlrev_b32_e32 v60, 8, v52
	v_lshlrev_b32_e32 v52, 2, v52
	v_and_b32_e32 v52, 12, v52
	v_mfma_f32_16x16x32_f16 v[44:47], v[56:59], v[6:9], v[44:47]
	v_or_b32_e32 v62, v52, v61
	v_bitop3_b32 v52, v236, v52, v61 bitop3:0x1e
	v_lshl_or_b32 v63, v52, 4, v60
	s_waitcnt lgkmcnt(2)
	v_mfma_f32_16x16x32_f16 v[44:47], v[72:75], v[2:5], v[44:47]
	ds_read_b128 v[52:55], v63
	v_bitop3_b32 v56, v236, v62, 4 bitop3:0x36
	v_lshl_or_b32 v84, v56, 4, v60
	s_waitcnt lgkmcnt(2)
	v_mfma_f32_16x16x32_f16 v[44:47], v[76:79], v[40:43], v[44:47]
	ds_read_b128 v[56:59], v84
	v_bitop3_b32 v68, v236, v62, 8 bitop3:0x36
	v_lshl_or_b32 v85, v68, 4, v60
	s_waitcnt lgkmcnt(2)
	v_mfma_f32_16x16x32_f16 v[110:113], v[80:83], v[106:109], v[44:47]
	ds_read_b128 v[68:71], v63 offset:49152
	v_bitop3_b32 v62, v236, v62, 12 bitop3:0x36
	v_lshl_or_b32 v60, v62, 4, v60
	ds_read_b128 v[44:47], v85
	s_waitcnt lgkmcnt(3)
	v_mfma_f32_16x16x32_f16 v[52:55], v[52:55], v[22:25], 0
	ds_read_b128 v[72:75], v60
	ds_read_b128 v[76:79], v84 offset:49152
	v_mad_u32_u24 v105, v103, 3, 2
	v_lshlrev_b32_e32 v133, 4, v105
	s_waitcnt lgkmcnt(4)
	v_mfma_f32_16x16x32_f16 v[52:55], v[56:59], v[18:21], v[52:55]
	ds_read_b128 v[56:59], v85 offset:49152
	v_add_co_u32_e32 v114, vcc, s15, v88
	s_waitcnt lgkmcnt(3)
	v_mfma_f32_16x16x32_f16 v[44:47], v[44:47], v[14:17], v[52:55]
	v_addc_co_u32_e32 v115, vcc, 0, v89, vcc
	s_waitcnt lgkmcnt(2)
	v_mfma_f32_16x16x32_f16 v[44:47], v[72:75], v[10:13], v[44:47]
	ds_read_b128 v[52:55], v60 offset:49152
	v_add_u32_e32 v60, v133, v147
	v_lshlrev_b32_e32 v72, 8, v60
	v_lshlrev_b32_e32 v60, 2, v60
	v_mfma_f32_16x16x32_f16 v[44:47], v[68:71], v[6:9], v[44:47]
	v_and_b32_e32 v60, 12, v60
	v_or_b32_e32 v68, v60, v61
	v_bitop3_b32 v60, v236, v60, v61 bitop3:0x1e
	v_lshl_or_b32 v69, v60, 4, v72
	s_waitcnt lgkmcnt(2)
	v_mfma_f32_16x16x32_f16 v[44:47], v[76:79], v[2:5], v[44:47]
	ds_read_b128 v[60:63], v69
	v_bitop3_b32 v70, v236, v68, 4 bitop3:0x36
	v_lshl_or_b32 v70, v70, 4, v72
	s_waitcnt lgkmcnt(2)
	v_mfma_f32_16x16x32_f16 v[44:47], v[56:59], v[40:43], v[44:47]
	ds_read_b128 v[56:59], v70
	v_bitop3_b32 v71, v236, v68, 8 bitop3:0x36
	v_lshl_or_b32 v71, v71, 4, v72
	s_waitcnt lgkmcnt(1)
	v_mfma_f32_16x16x32_f16 v[22:25], v[60:63], v[22:25], 0
	v_bitop3_b32 v60, v236, v68, 12 bitop3:0x36
	v_lshl_or_b32 v68, v60, 4, v72
	ds_read_b32 v210, v209
	v_mfma_f32_16x16x32_f16 v[126:129], v[52:55], v[106:109], v[44:47]
	s_nop 2
	ds_read_b128 v[44:47], v71
	ds_read_b128 v[52:55], v69 offset:49152
	ds_read_b128 v[60:63], v70 offset:49152
	s_waitcnt lgkmcnt(4)
	v_mfma_f32_16x16x32_f16 v[18:21], v[56:59], v[18:21], v[22:25]
	ds_read_b128 v[56:59], v71 offset:49152
	s_nop 1
	ds_read_b128 v[22:25], v68
	s_waitcnt lgkmcnt(4)
	v_mfma_f32_16x16x32_f16 v[14:17], v[44:47], v[14:17], v[18:21]
	v_add_co_u32_e32 v44, vcc, s5, v88
	s_movk_i32 s5, 0x3000
	s_nop 0
	ds_read_b128 v[18:21], v68 offset:49152
	s_waitcnt lgkmcnt(1)
	v_mfma_f32_16x16x32_f16 v[10:13], v[22:25], v[10:13], v[14:17]
	v_addc_co_u32_e32 v45, vcc, 0, v89, vcc
	global_load_dwordx4 v[84:87], v[114:115], off offset:1024
	global_load_dwordx4 v[80:83], v[114:115], off offset:2048
	global_load_dwordx4 v[92:95], v[44:45], off offset:-4096
	global_load_dwordx4 v[76:79], v[44:45], off
	v_mfma_f32_16x16x32_f16 v[6:9], v[52:55], v[6:9], v[10:13]
	global_load_dwordx4 v[72:75], v[44:45], off offset:1024
	global_load_dwordx4 v[68:71], v[44:45], off offset:2048
	global_load_dwordx4 v[52:55], v[44:45], off offset:3072
	v_mov_b32_e32 v13, 0xff61b1e6
	v_mfma_f32_16x16x32_f16 v[2:5], v[60:63], v[2:5], v[6:9]
	s_nop 2
	v_add_co_u32_e32 v6, vcc, s5, v88
	v_mfma_f32_16x16x32_f16 v[2:5], v[56:59], v[40:43], v[2:5]
	s_nop 0
	v_addc_co_u32_e32 v7, vcc, 0, v89, vcc
	global_load_dwordx4 v[88:91], v[114:115], off offset:3072
	global_load_dwordx4 v[60:63], v[6:7], off
	global_load_dwordx4 v[56:59], v[6:7], off offset:1024
	global_load_dwordx4 v[44:47], v[6:7], off offset:2048
	global_load_dwordx4 v[40:43], v[6:7], off offset:3072
	s_waitcnt lgkmcnt(0)
	v_mfma_f32_16x16x32_f16 v[16:19], v[18:21], v[106:109], v[2:5]
	s_mov_b32 s5, 0xff61b1e6
	s_nop 0
	v_or_b32_e32 v3, s14, v146
	v_mov_b32_e32 v4, 0x7df
	v_med3_u32 v3, v3, 32, v4
	v_or_b32_e32 v4, v97, v102
	v_sub_u32_e32 v3, v4, v3
	v_add_f32_e32 v2, s32, v210
	v_add_u32_e32 v3, 32, v3
	v_mad_u32_u24 v4, v103, 48, v3
	s_movk_i32 s4, 0x41
	v_add_f32_e32 v5, v2, v110
	v_mul_f32_e32 v5, 0x3db8aa3b, v5
	v_cmp_gt_u32_e32 vcc, s4, v4
	v_add_u32_e32 v6, 1, v4
	v_add_f32_e32 v7, v2, v111
	v_cndmask_b32_e32 v5, v13, v5, vcc
	v_mul_f32_e32 v7, 0x3db8aa3b, v7
	v_cmp_gt_u32_e32 vcc, s4, v6
	v_add_u32_e32 v8, 2, v4
	v_add_f32_e32 v9, v2, v112
	v_cndmask_b32_e32 v6, v13, v7, vcc
	v_mul_f32_e32 v9, 0x3db8aa3b, v9
	v_cmp_gt_u32_e32 vcc, s4, v8
	v_add_u32_e32 v4, 3, v4
	v_max3_f32 v7, v5, s5, v6
	v_cndmask_b32_e32 v8, v13, v9, vcc
	v_add_f32_e32 v9, v2, v113
	v_mul_f32_e32 v9, 0x3db8aa3b, v9
	v_cmp_gt_u32_e32 vcc, s4, v4
	v_add_u32_e32 v11, v3, v132
	v_add_f32_e32 v12, v2, v127
	v_cndmask_b32_e32 v10, v13, v9, vcc
	v_max3_f32 v4, v7, v8, v10
	v_add_f32_e32 v7, v2, v126
	v_mul_f32_e32 v7, 0x3db8aa3b, v7
	v_cmp_gt_u32_e32 vcc, s4, v11
	v_add_u32_e32 v9, 1, v11
	v_mul_f32_e32 v12, 0x3db8aa3b, v12
	v_cndmask_b32_e32 v7, v13, v7, vcc
	v_cmp_gt_u32_e32 vcc, s4, v9
	v_add_f32_e32 v14, v2, v128
	v_mul_f32_e32 v14, 0x3db8aa3b, v14
	v_cndmask_b32_e32 v9, v13, v12, vcc
	v_add_u32_e32 v12, 2, v11
	v_cmp_gt_u32_e32 vcc, s4, v12
	v_add_u32_e32 v11, 3, v11
	v_add_u32_e32 v3, v3, v133
	v_cndmask_b32_e32 v12, v13, v14, vcc
	v_add_f32_e32 v14, v2, v129
	v_mul_f32_e32 v14, 0x3db8aa3b, v14
	v_cmp_gt_u32_e32 vcc, s4, v11
	v_add_f32_e32 v11, v2, v16
	v_mul_f32_e32 v11, 0x3db8aa3b, v11
	v_cndmask_b32_e32 v15, v13, v14, vcc
	v_cmp_gt_u32_e32 vcc, s4, v3
	v_add_u32_e32 v14, 1, v3
	v_add_f32_e32 v16, v2, v17
	v_cndmask_b32_e32 v11, v13, v11, vcc
	v_mul_f32_e32 v16, 0x3db8aa3b, v16
	v_cmp_gt_u32_e32 vcc, s4, v14
	v_add_f32_e32 v17, v2, v18
	v_max3_f32 v4, v4, v7, v9
	v_cndmask_b32_e32 v14, v13, v16, vcc
	v_add_u32_e32 v16, 2, v3
	v_mul_f32_e32 v17, 0x3db8aa3b, v17
	v_cmp_gt_u32_e32 vcc, s4, v16
	v_add_u32_e32 v3, 3, v3
	v_add_f32_e32 v2, v2, v19
	v_max3_f32 v4, v4, v12, v15
	v_cndmask_b32_e32 v16, v13, v17, vcc
	v_mul_f32_e32 v2, 0x3db8aa3b, v2
	v_cmp_gt_u32_e32 vcc, s4, v3
	v_max3_f32 v4, v4, v11, v14
	v_lshlrev_b32_e32 v126, 5, v99
	v_cndmask_b32_e32 v17, v13, v2, vcc
	v_max3_f32 v2, v4, v16, v17
	v_mov_b32_e32 v3, v2
	v_lshlrev_b32_e32 v127, 2, v119
	v_lshrrev_b32_e32 v4, 7, v0
	v_cmp_gt_u32_e32 vcc, 16, v98
	v_permlane16_swap_b32_e32 v3, v2
	v_max_f32_e32 v2, v2, v3
	v_mov_b32_e32 v3, v2
	s_nop 1
	v_permlane32_swap_b32_e32 v3, v2
	v_max_f32_e32 v13, v2, v3
	v_and_b32_e32 v2, 0x180, v0
	v_or_b32_e32 v2, 0x23400, v2
	v_lshlrev_b32_e32 v3, 2, v100
	s_and_saveexec_b64 s[4:5], vcc
	v_lshlrev_b32_e32 v18, 6, v103
	v_add3_u32 v18, v2, v18, v3
	ds_write_b32 v18, v13
	s_or_b64 exec, exec, s[4:5]
	v_lshlrev_b32_e32 v18, 4, v103
	v_bitop3_b32 v19, v18, 16, v100 bitop3:0x36
	v_lshl_add_u32 v2, v19, 2, v2
	s_waitcnt lgkmcnt(0)
	s_barrier
	ds_read_b32 v19, v2
	v_max_f32_e32 v13, v13, v13
	v_mul_u32_u24_e32 v20, 0xd00, v4
	v_or_b32_e32 v2, 1, v124
	s_waitcnt lgkmcnt(0)
	v_max_f32_e32 v19, v19, v19
	v_max_f32_e32 v19, v13, v19
	v_sub_f32_e32 v5, v5, v19
	v_exp_f32_e32 v5, v5
	v_sub_f32_e32 v6, v6, v19
	v_exp_f32_e32 v6, v6
	v_sub_f32_e32 v8, v8, v19
	v_mul_u32_u24_e32 v13, 0xd0, v100
	v_exp_f32_e32 v8, v8
	v_sub_f32_e32 v10, v10, v19
	v_add3_u32 v20, v13, v20, v29
	v_exp_f32_e32 v10, v10
	v_or_b32_e32 v22, 0x20000, v20
	v_add_f32_e32 v20, 0, v5
	v_add_f32_e32 v20, v20, v6
	v_add_f32_e32 v20, v20, v8
	v_add_f32_e32 v23, v20, v10
	v_cvt_pk_f16_f32 v21, v8, v10
	v_cvt_pk_f16_f32 v20, v5, v6
	v_mad_u32_u24 v5, v103, s16, v22
	ds_write_b64 v5, v[20:21]
	v_sub_f32_e32 v5, v7, v19
	v_exp_f32_e32 v5, v5
	v_sub_f32_e32 v6, v9, v19
	v_exp_f32_e32 v6, v6
	v_sub_f32_e32 v7, v12, v19
	v_exp_f32_e32 v7, v7
	v_sub_f32_e32 v8, v15, v19
	v_exp_f32_e32 v8, v8
	v_sub_f32_e32 v10, v11, v19
	v_add_f32_e32 v9, v23, v5
	v_exp_f32_e32 v10, v10
	v_sub_f32_e32 v11, v14, v19
	v_add_f32_e32 v9, v9, v6
	v_exp_f32_e32 v11, v11
	v_sub_f32_e32 v12, v16, v19
	v_add_f32_e32 v9, v9, v7
	v_exp_f32_e32 v12, v12
	v_sub_f32_e32 v14, v17, v19
	v_add_f32_e32 v9, v9, v8
	v_exp_f32_e32 v14, v14
	v_add_f32_e32 v9, v9, v10
	v_add_f32_e32 v9, v9, v11
	v_add_f32_e32 v9, v9, v12
	v_add_f32_e32 v9, v9, v14
	v_mov_b32_e32 v15, v9
	v_cvt_pk_f16_f32 v7, v7, v8
	v_cvt_pk_f16_f32 v6, v5, v6
	v_lshl_add_u32 v5, v104, 5, v22
	ds_write_b64 v5, v[6:7]
	v_permlane16_swap_b32_e32 v15, v9
	v_add_f32_e32 v5, v9, v15
	v_mov_b32_e32 v6, v5
	s_movk_i32 s7, 0xd00
	s_mov_b32 s6, 0x20000
	v_cvt_pk_f16_f32 v9, v12, v14
	v_cvt_pk_f16_f32 v8, v10, v11
	v_lshl_add_u32 v7, v105, 5, v22
	ds_write_b64 v7, v[8:9]
	v_permlane32_swap_b32_e32 v6, v5
	s_and_saveexec_b64 s[4:5], vcc
	s_cbranch_execz .LBB1_4
	v_lshlrev_b32_e32 v4, 5, v4
	v_or_b32_e32 v7, v18, v100
	v_lshlrev_b32_e32 v4, 2, v4
	v_lshlrev_b32_e32 v7, 2, v7
	s_mov_b32 s8, 0x23600
	v_add3_u32 v4, v7, v4, s8
	v_add_f32_e32 v5, v5, v6
	ds_write_b32 v4, v5

amdhsa.kernels:
  - .agpr_count:     16
    .args:
      - .actual_access:  read_only
        .address_space:  global
        .offset:         0
        .size:           8
        .value_kind:     global_buffer
      - .actual_access:  read_only
        .address_space:  global
        .offset:         8
        .size:           8
        .value_kind:     global_buffer
      - .actual_access:  read_only
        .address_space:  global
        .offset:         16
        .size:           8
        .value_kind:     global_buffer
      - .actual_access:  read_only
        .address_space:  global
        .offset:         24
        .size:           8
        .value_kind:     global_buffer
      - .actual_access:  read_only
        .address_space:  global
        .offset:         32
        .size:           8
        .value_kind:     global_buffer
      - .actual_access:  read_only
        .address_space:  global
        .offset:         40
        .size:           8
        .value_kind:     global_buffer
      - .actual_access:  write_only
        .address_space:  global
        .offset:         48
        .size:           8
        .value_kind:     global_buffer
      - .actual_access:  write_only
        .address_space:  global
        .offset:         56
        .size:           8
        .value_kind:     global_buffer
      - .actual_access:  write_only
        .address_space:  global
        .offset:         64
        .size:           8
        .value_kind:     global_buffer
      - .actual_access:  write_only
        .address_space:  global
        .offset:         72
        .size:           8
        .value_kind:     global_buffer
      - .actual_access:  write_only
        .address_space:  global
        .offset:         80
        .size:           8
        .value_kind:     global_buffer
      - .actual_access:  write_only
        .address_space:  global
        .offset:         88
        .size:           8
        .value_kind:     global_buffer
    .group_segment_fixed_size: 50176
    .kernarg_segment_align: 8
    .kernarg_segment_size: 96
    .language:       OpenCL C
    .language_version:
      - 2
      - 0
    .max_flat_workgroup_size: 256
    .name:           _Z7na_prepPKfS0_S0_S0_S0_S0_PDF16_PhS1_PfS3_S3_
    .private_segment_fixed_size: 0
    .sgpr_count:     23
    .sgpr_spill_count: 0
    .symbol:         _Z7na_prepPKfS0_S0_S0_S0_S0_PDF16_PhS1_PfS3_S3_.kd
    .uniform_work_group_size: 1
    .uses_dynamic_stack: false
    .vgpr_count:     116
    .vgpr_spill_count: 0
    .wavefront_size: 64
  - .agpr_count:     0
    .args:
      - .address_space:  global
        .offset:         0
        .size:           8
        .value_kind:     global_buffer
      - .actual_access:  read_only
        .address_space:  global
        .offset:         8
        .size:           8
        .value_kind:     global_buffer
      - .actual_access:  read_only
        .address_space:  global
        .offset:         16
        .size:           8
        .value_kind:     global_buffer
      - .actual_access:  read_only
        .address_space:  global
        .offset:         24
        .size:           8
        .value_kind:     global_buffer
      - .actual_access:  read_only
        .address_space:  global
        .offset:         32
        .size:           8
        .value_kind:     global_buffer
      - .actual_access:  read_only
        .address_space:  global
        .offset:         40
        .size:           8
        .value_kind:     global_buffer
      - .actual_access:  read_only
        .address_space:  global
        .offset:         48
        .size:           8
        .value_kind:     global_buffer
      - .actual_access:  write_only
        .address_space:  global
        .offset:         56
        .size:           8
        .value_kind:     global_buffer
    .group_segment_fixed_size: 162048
    .kernarg_segment_align: 8
    .kernarg_segment_size: 64
    .language:       OpenCL C
    .language_version:
      - 2
      - 0
    .max_flat_workgroup_size: 512
    .name:           _Z7na_mainPKDF16_PKhS0_PKfS4_S4_S4_Pf
    .private_segment_fixed_size: 0
    .sgpr_count:     43
    .sgpr_spill_count: 0
    .symbol:         _Z7na_mainPKDF16_PKhS0_PKfS4_S4_S4_Pf.kd
    .uniform_work_group_size: 1
    .uses_dynamic_stack: false
    .vgpr_count:     252
    .vgpr_spill_count: 0
    .wavefront_size: 64
